# Fourier stage A output: each wave transposes its 32-row tile through a private LDS staging area so global stores are 16 B per lane with 8 adjacent lanes covering a full 128 B line (8 stores instead of
# speedup vs baseline: 1.0043x; 1.0043x over previous
; #define LAS __attribute__((address_space(3)))
;     __device__ __forceinline__ bf16_t* dft() const { return (bf16_t*)(ws + WS_DFT); }
; #define FA_LOAD(u) do { const int _b = (u) >> 8, _n2 = ((u) >> 2) & 63, _cb = (u) & 3; \
;         _Pragma("unroll") for (int _q = 0; _q < 4; ++_q) { const int _n1 = (_q >> 1) * 64 + (_q & 1) * 32 + sr; \
;             pf[_q] = *(const bf16x8*)(F.proj() + (size_t)(_b * SEQ + 64 * _n1 + _n2) * INW + C_FX + _cb * 128 + sc); } } while (0)
; __device__ __forceinline__ void phase_fft_a(const Frame& F) {
;     const int tid = F.tid, wid = F.wid, lane = F.lane, r32 = lane & 31, hi = lane >> 5;
;     LAS char* Vt = (LAS char*)F.lds;
;     const int sr = tid >> 4, sc = (tid & 15) * 8;
;     const int rb = wid & 3, chh = wid >> 2, k1 = 32 * rb + r32;
;     const bf16_t* dc = F.dft(); const bf16_t* ds = F.dft() + 16384;
;     const int NU = NB * 64 * 4;
;     bf16x8 pf[4];
;     ...
;     int u = F.wg, par = 0;
;     if (u < NU) FA_LOAD(u);
.LBB0_324:
	s_or_b64 exec, exec, s[44:45]
	v_readlane_b32 s8, v252, 54
	v_mov_b32_e32 v2, v0
	v_readlane_b32 s9, v252, 55
	s_andn2_b64 vcc, exec, s[8:9]
	v_readfirstlane_b32 s0, v2
	v_readlane_b32 s31, v254, 5
	s_cbranch_vccnz .LBB0_331
	s_lshr_b32 s1, s0, 1
	v_ashrrev_i32_e32 v5, 4, v2
	s_and_b32 s1, s1, 0x60
	v_lshlrev_b32_e32 v1, 6, v5
	v_readlane_b32 s2, v252, 56
	s_add_u32 s8, s56, 0xc8000
	s_addc_u32 s9, s57, 0
	v_add_u32_e32 v6, s2, v1
	v_ashrrev_i32_e32 v7, 31, v6
	s_add_u32 s18, s56, 0xc0000
	v_lshlrev_b32_e32 v3, 3, v2
	v_lshlrev_b64 v[8:9], 13, v[6:7]
	v_readlane_b32 s2, v252, 57
	v_add_u32_e32 v10, 0x800, v6
	s_addc_u32 s19, s57, 0
	v_and_b32_e32 v4, 0x78, v3
	v_lshl_add_u64 v[8:9], s[56:57], 0, v[8:9]
	s_lshl_b32 s76, s2, 1
	v_ashrrev_i32_e32 v11, 31, v10
	v_lshl_add_u64 v[8:9], v[8:9], 0, s[76:77]
	v_lshlrev_b32_e32 v146, 1, v4
	v_lshlrev_b64 v[10:11], 13, v[10:11]
	v_lshl_add_u64 v[8:9], v[8:9], 0, v[146:147]
	s_mov_b32 s2, 0x1c317000
	v_lshl_add_u64 v[10:11], s[56:57], 0, v[10:11]
	v_add_co_u32_e32 v8, vcc, s2, v8
	v_lshl_add_u64 v[10:11], v[10:11], 0, s[76:77]
	s_nop 0
	v_addc_co_u32_e32 v9, vcc, 0, v9, vcc
	v_lshl_add_u64 v[10:11], v[10:11], 0, v[146:147]
	v_add_co_u32_e32 v10, vcc, s2, v10
	v_and_or_b32 v120, v2, 31, s1
	s_nop 0
	v_addc_co_u32_e32 v11, vcc, 0, v11, vcc
	global_load_dwordx4 v[66:69], v[8:9], off offset:2304
	global_load_dwordx4 v[70:73], v[10:11], off offset:2304
	v_add_u32_e32 v8, 0x1000, v6
	v_ashrrev_i32_e32 v9, 31, v8
	v_lshlrev_b64 v[8:9], 13, v[8:9]
	v_add_u32_e32 v6, 0x1800, v6
	v_lshl_add_u64 v[8:9], s[56:57], 0, v[8:9]
	v_ashrrev_i32_e32 v7, 31, v6
	v_lshl_add_u64 v[8:9], v[8:9], 0, s[76:77]
	v_lshlrev_b64 v[6:7], 13, v[6:7]
	v_lshl_add_u64 v[8:9], v[8:9], 0, v[146:147]
	v_lshl_add_u64 v[6:7], s[56:57], 0, v[6:7]
	v_add_co_u32_e32 v8, vcc, s2, v8
	v_lshl_add_u64 v[6:7], v[6:7], 0, s[76:77]
	s_nop 0
	v_addc_co_u32_e32 v9, vcc, 0, v9, vcc
	v_lshl_add_u64 v[6:7], v[6:7], 0, v[146:147]
	v_add_co_u32_e32 v6, vcc, s2, v6
	s_ashr_i32 s1, s0, 8
	s_nop 0
	v_addc_co_u32_e32 v7, vcc, 0, v7, vcc
	global_load_dwordx4 v[74:77], v[8:9], off offset:2304
	global_load_dwordx4 v[78:81], v[6:7], off offset:2304
	v_lshrrev_b32_e32 v7, 1, v5
	v_and_b32_e32 v9, 3, v5
	v_and_or_b32 v7, v7, 4, v9
	v_lshlrev_b32_e32 v121, 6, v7
	v_lshlrev_b32_e32 v7, 4, v2
	v_bfe_u32 v6, v2, 5, 1
	v_and_b32_e32 v122, 48, v7
	v_and_b32_e32 v7, 0xc0, v7
	v_lshlrev_b32_e32 v2, 1, v2
	v_bfe_u32 v8, v3, 5, 2
	v_and_b32_e32 v2, 32, v2
	v_lshl_or_b32 v7, s1, 10, v7
	v_and_b32_e32 v3, 0x118, v3
	v_or3_b32 v123, v7, v3, v2
	v_and_b32_e32 v3, 0xfffff0, v5
	v_lshlrev_b32_e32 v7, 1, v5
	v_and_or_b32 v3, v7, 8, v3
	v_lshrrev_b32_e32 v3, 1, v3
	v_or_b32_e32 v3, v3, v8
	v_lshlrev_b32_e32 v124, 9, v3
	v_add_u32_e32 v3, 32, v5
	v_and_b32_e32 v5, 0xfffff0, v3
	v_lshlrev_b32_e32 v3, 1, v3
	v_and_or_b32 v3, v3, 8, v5
	v_lshrrev_b32_e32 v3, 1, v3
	v_or_b32_e32 v3, v3, v8
	v_lshlrev_b32_e32 v125, 9, v3
	v_lshlrev_b32_e32 v3, 8, v120
	v_lshl_or_b32 v146, v6, 4, v3
	v_lshlrev_b32_e32 v2, 2, v6
	v_or_b32_e32 v6, 32, v146
	v_mov_b32_e32 v7, v147
	v_lshl_add_u64 v[86:87], s[18:19], 0, v[6:7]
	v_lshl_add_u64 v[88:89], s[8:9], 0, v[6:7]
	v_or_b32_e32 v6, 64, v146
	s_lshl_b32 s28, s1, 6
	v_lshl_add_u64 v[90:91], s[18:19], 0, v[6:7]
	v_lshl_add_u64 v[92:93], s[8:9], 0, v[6:7]
	v_or_b32_e32 v6, 0x60, v146
	s_ashr_i32 s29, s28, 31
	v_lshl_add_u64 v[94:95], s[18:19], 0, v[6:7]
	v_lshl_add_u64 v[96:97], s[8:9], 0, v[6:7]
	v_or_b32_e32 v6, 0x80, v146
	v_lshl_add_u64 v[98:99], s[18:19], 0, v[6:7]
	v_lshl_add_u64 v[100:101], s[8:9], 0, v[6:7]
	v_or_b32_e32 v6, 0xa0, v146
	s_add_u32 s40, s56, 0xb0000
	v_lshl_add_u64 v[82:83], s[18:19], 0, v[146:147]
	v_lshl_add_u64 v[84:85], s[8:9], 0, v[146:147]
	v_lshl_add_u64 v[102:103], s[18:19], 0, v[6:7]
	v_lshl_add_u64 v[104:105], s[8:9], 0, v[6:7]
	v_or_b32_e32 v6, 0xc0, v146
	v_or_b32_e32 v146, 0xe0, v146
	s_addc_u32 s41, s57, 0
	v_lshlrev_b32_e32 v9, 7, v120
	v_lshl_add_u64 v[108:109], s[8:9], 0, v[6:7]
	v_lshl_add_u64 v[112:113], s[8:9], 0, v[146:147]
	s_add_u32 s24, s56, 0x3d316100
	v_readlane_b32 s8, v254, 62
	s_mov_b32 s0, 0
	v_lshl_add_u64 v[106:107], s[18:19], 0, v[6:7]
	v_lshl_add_u64 v[110:111], s[18:19], 0, v[146:147]
	s_addc_u32 s25, s57, 0
	v_lshlrev_b32_e32 v114, 1, v4
	v_lshlrev_b32_e32 v126, 2, v9
	v_lshlrev_b32_e32 v146, 1, v2
	v_readlane_b32 s1, v253, 60
	v_readlane_b32 s22, v253, 15
	s_mov_b32 s23, s8
	v_readlane_b32 s9, v254, 63
	v_and_b32_e32 v176, 31, v0
	v_mul_u32_u24_e32 v176, 0x110, v176
	v_bfe_u32 v177, v0, 5, 1
	v_lshl_add_u32 v176, v177, 3, v176
	v_lshrrev_b32_e32 v177, 6, v0
	v_mul_u32_u24_e32 v177, 0x2200, v177
	v_add_u32_e32 v177, 0x10000, v177
	v_add_u32_e32 v176, v176, v177
	v_bfe_u32 v178, v0, 3, 3
	v_mul_u32_u24_e32 v178, 0x110, v178
	v_add_u32_e32 v177, v177, v178
	v_and_b32_e32 v178, 7, v0
	v_lshl_add_u32 v177, v178, 4, v177
	v_bfe_u32 v120, v0, 3, 3
	v_bfe_u32 v178, v0, 6, 2
	v_lshl_or_b32 v120, v178, 5, v120
	v_and_b32_e32 v146, 7, v0
	v_lshlrev_b32_e32 v146, 4, v146
	s_branch .LBB0_327
;     __device__ __forceinline__ float* tw() const { return (float*)(ws + WS_TW); }
;     __device__ __forceinline__ bf16_t* zm() const { return (bf16_t*)(ws + WS_ZM); }
; __device__ __forceinline__ int v_rd_base(int lane) { return ((lane & 3) << 3) | (((lane >> 2) & 3) << 6) | (((lane >> 4) & 1) << 5) | (((lane >> 5) & 1) << 8); }
; __device__ __forceinline__ void phase_fft_a(const Frame& F) {
;     ...
;         f32x16 zc[2] = {f32x16{}, f32x16{}}, zs[2] = {f32x16{}, f32x16{}};
; #pragma unroll
;         for (int t = 0; t < 2; ++t) {
;             bf16x8 bc[4], bs[4];
; #pragma unroll
;             for (int ks = 0; ks < 4; ++ks) { const int o = k1 * 128 + t * 64 + ks * 16 + hi * 8; bc[ks] = *(const bf16x8*)(dc + o); bs[ks] = *(const bf16x8*)(ds + o); }
;             const int vb = (int)(uintptr_t)img + t * 16384 + ff::v_rd_base(lane) + chh * 1024;
;             ff::xt_two<0>(zc[0], zs[0], vb, bc, bs);
;             ff::xt_two<1>(zc[1], zs[1], vb, bc, bs);
;         }
;         const f32x2 t2 = *(const f32x2*)(F.tw() + (size_t)(k1 * 64 + n2) * 2);
;         bf16_t* zp = F.zm() + (size_t)((b * 128 + k1) * 64 + n2) * DM + cb * 128 + 64 * chh + 4 * hi;
.LBB0_326:
	global_load_dwordx4 v[2:5], v[82:83], off
	global_load_dwordx4 v[18:21], v[84:85], off
	global_load_dwordx4 v[116:119], v[86:87], off
	global_load_dwordx4 v[128:131], v[88:89], off
	global_load_dwordx4 v[132:135], v[90:91], off
	global_load_dwordx4 v[136:139], v[92:93], off
	global_load_dwordx4 v[140:143], v[94:95], off
	global_load_dwordx4 v[148:151], v[96:97], off
	v_add_u32_e32 v115, s30, v123
	ds_read_b64_tr_b16 v[6:7], v115 offset:0
	ds_read_b64_tr_b16 v[8:9], v115 offset:0x800
	ds_read_b64_tr_b16 v[10:11], v115 offset:0x1000
	ds_read_b64_tr_b16 v[12:13], v115 offset:0x1800
	ds_read_b64_tr_b16 v[14:15], v115 offset:0x2000
	ds_read_b64_tr_b16 v[16:17], v115 offset:0x2800
	ds_read_b64_tr_b16 v[22:23], v115 offset:0x3000
	ds_read_b64_tr_b16 v[24:25], v115 offset:0x3800
	s_waitcnt lgkmcnt(0)
	s_bfe_u32 s8, s23, 0x60002
	s_waitcnt vmcnt(7)
	v_mfma_f32_32x32x16_bf16 v[34:49], v[6:9], v[2:5], 0
	s_waitcnt vmcnt(6)
	v_mfma_f32_32x32x16_bf16 v[50:65], v[6:9], v[18:21], 0
	s_waitcnt vmcnt(5)
	v_mfma_f32_32x32x16_bf16 v[34:49], v[10:13], v[116:119], v[34:49]
	s_waitcnt vmcnt(4)
	v_mfma_f32_32x32x16_bf16 v[50:65], v[10:13], v[128:131], v[50:65]
	s_waitcnt vmcnt(3)
	v_mfma_f32_32x32x16_bf16 v[34:49], v[14:17], v[132:135], v[34:49]
	s_waitcnt vmcnt(2)
	v_mfma_f32_32x32x16_bf16 v[50:65], v[14:17], v[136:139], v[50:65]
	s_waitcnt vmcnt(1)
	v_mfma_f32_32x32x16_bf16 v[34:49], v[22:25], v[140:143], v[34:49]
	s_waitcnt vmcnt(0)
	v_mfma_f32_32x32x16_bf16 v[50:65], v[22:25], v[148:151], v[50:65]
	ds_read_b64_tr_b16 v[22:23], v115 offset:0x200
	ds_read_b64_tr_b16 v[24:25], v115 offset:0xa00
	ds_read_b64_tr_b16 v[152:153], v115 offset:0x1200
	ds_read_b64_tr_b16 v[154:155], v115 offset:0x1a00
	ds_read_b64_tr_b16 v[156:157], v115 offset:0x2200
	ds_read_b64_tr_b16 v[158:159], v115 offset:0x2a00
	ds_read_b64_tr_b16 v[160:161], v115 offset:0x3200
	ds_read_b64_tr_b16 v[162:163], v115 offset:0x3a00
	s_waitcnt lgkmcnt(0)
	s_nop 0
	v_mfma_f32_32x32x16_bf16 v[2:17], v[22:25], v[2:5], 0
	v_add_u32_e32 v115, 0x4000, v115
	v_mfma_f32_32x32x16_bf16 v[18:33], v[22:25], v[18:21], 0
	v_mfma_f32_32x32x16_bf16 v[2:17], v[152:155], v[116:119], v[2:17]
	v_mfma_f32_32x32x16_bf16 v[18:33], v[152:155], v[128:131], v[18:33]
	v_mfma_f32_32x32x16_bf16 v[2:17], v[156:159], v[132:135], v[2:17]
	v_mfma_f32_32x32x16_bf16 v[18:33], v[156:159], v[136:139], v[18:33]
	v_mfma_f32_32x32x16_bf16 v[2:17], v[160:163], v[140:143], v[2:17]
	v_mfma_f32_32x32x16_bf16 v[18:33], v[160:163], v[148:151], v[18:33]
	global_load_dwordx4 v[116:119], v[98:99], off
	global_load_dwordx4 v[128:131], v[100:101], off
	global_load_dwordx4 v[132:135], v[102:103], off
	global_load_dwordx4 v[136:139], v[104:105], off
	global_load_dwordx4 v[140:143], v[106:107], off
	global_load_dwordx4 v[148:151], v[108:109], off
	global_load_dwordx4 v[152:155], v[110:111], off
	global_load_dwordx4 v[156:159], v[112:113], off
	ds_read_b64_tr_b16 v[160:161], v115 offset:0
	ds_read_b64_tr_b16 v[162:163], v115 offset:0x800
	ds_read_b64_tr_b16 v[164:165], v115 offset:0x1000
	ds_read_b64_tr_b16 v[166:167], v115 offset:0x1800
	ds_read_b64_tr_b16 v[168:169], v115 offset:0x2000
	ds_read_b64_tr_b16 v[170:171], v115 offset:0x2800
	ds_read_b64_tr_b16 v[172:173], v115 offset:0x3000
	ds_read_b64_tr_b16 v[174:175], v115 offset:0x3800
	s_waitcnt lgkmcnt(0)
	s_waitcnt vmcnt(7)
	v_mfma_f32_32x32x16_bf16 v[34:49], v[160:163], v[116:119], v[34:49]
	s_waitcnt vmcnt(6)
	v_mfma_f32_32x32x16_bf16 v[50:65], v[160:163], v[128:131], v[50:65]
	ds_read_b64_tr_b16 v[160:161], v115 offset:0x200
	ds_read_b64_tr_b16 v[162:163], v115 offset:0xa00
	s_waitcnt vmcnt(5)
	v_mfma_f32_32x32x16_bf16 v[34:49], v[164:167], v[132:135], v[34:49]
	s_waitcnt vmcnt(4)
	v_mfma_f32_32x32x16_bf16 v[50:65], v[164:167], v[136:139], v[50:65]
	ds_read_b64_tr_b16 v[164:165], v115 offset:0x1200
	ds_read_b64_tr_b16 v[166:167], v115 offset:0x1a00
	s_waitcnt vmcnt(3)
	v_mfma_f32_32x32x16_bf16 v[34:49], v[168:171], v[140:143], v[34:49]
	s_waitcnt vmcnt(2)
	v_mfma_f32_32x32x16_bf16 v[50:65], v[168:171], v[148:151], v[50:65]
	ds_read_b64_tr_b16 v[168:169], v115 offset:0x2200
	ds_read_b64_tr_b16 v[170:171], v115 offset:0x2a00
	s_waitcnt vmcnt(1)
	v_mfma_f32_32x32x16_bf16 v[34:49], v[172:175], v[152:155], v[34:49]
	s_waitcnt vmcnt(0)
	v_mfma_f32_32x32x16_bf16 v[50:65], v[172:175], v[156:159], v[50:65]
	ds_read_b64_tr_b16 v[172:173], v115 offset:0x3200
	ds_read_b64_tr_b16 v[174:175], v115 offset:0x3a00
	s_waitcnt lgkmcnt(0)
	v_lshl_or_b32 v115, s8, 3, v126
	v_mfma_f32_32x32x16_bf16 v[2:17], v[160:163], v[116:119], v[2:17]
	global_load_dwordx2 v[116:117], v115, s[40:41]
	s_lshr_b32 s9, s23, 1
	s_and_b32 s9, s9, 0x3ffff80
	v_or_b32_e32 v115, s9, v120
	v_lshl_or_b32 v118, v115, 6, s8
	v_ashrrev_i32_e32 v119, 31, v118
	s_and_b32 s22, s22, 0x180
	v_mfma_f32_32x32x16_bf16 v[18:33], v[160:163], v[128:131], v[18:33]
	v_lshlrev_b64 v[118:119], 11, v[118:119]
	v_mov_b32_e32 v128, v34
	v_mov_b32_e32 v129, v50
	v_mov_b32_e32 v130, v50
	v_mov_b32_e32 v131, v34
	v_mov_b32_e32 v50, v35
	v_mov_b32_e32 v34, v51
	v_mfma_f32_32x32x16_bf16 v[2:17], v[164:167], v[132:135], v[2:17]
	v_mov_b32_e32 v132, v36
	v_mov_b32_e32 v133, v52
	s_lshl_b32 s76, s22, 1
	v_lshl_add_u64 v[118:119], s[24:25], 0, v[118:119]
	v_mov_b32_e32 v134, v52
	v_mov_b32_e32 v135, v36
	v_mov_b32_e32 v52, v37
	v_mov_b32_e32 v36, v53
	v_lshl_add_u64 v[118:119], v[118:119], 0, s[76:77]
	v_mfma_f32_32x32x16_bf16 v[18:33], v[164:167], v[136:139], v[18:33]
	v_mov_b32_e32 v136, v38
	v_mov_b32_e32 v137, v54
	v_mov_b32_e32 v138, v54
	v_mov_b32_e32 v139, v38
	v_mov_b32_e32 v54, v39
	v_mov_b32_e32 v38, v55
	v_lshl_add_u64 v[118:119], s[28:29], 1, v[118:119]
	v_mfma_f32_32x32x16_bf16 v[2:17], v[168:171], v[140:143], v[2:17]
	v_mov_b32_e32 v140, v40
	v_mov_b32_e32 v141, v56
	v_mov_b32_e32 v142, v56
	v_mov_b32_e32 v56, v41
	v_mov_b32_e32 v143, v40
	v_mov_b32_e32 v40, v57
	v_lshl_add_u64 v[118:119], v[118:119], 0, v[146:147]
	v_mfma_f32_32x32x16_bf16 v[18:33], v[168:171], v[148:151], v[18:33]
	s_xor_b32 s0, s0, 1
	s_add_i32 s1, s1, s31
	s_andn2_b64 vcc, exec, s[18:19]
	s_mov_b32 s22, s7
	s_mov_b32 s23, s2
	s_waitcnt vmcnt(0)
; __device__ __forceinline__ unsigned cvt_pk_bf16(float lo, float hi) { unsigned r; asm volatile("v_cvt_pk_bf16_f32 %0, %1, %2" : "=v"(r) : "v"(lo), "v"(hi)); return r; }
; __device__ __forceinline__ void phase_fft_a(const Frame& F) {
;     ...
; #pragma unroll
;         for (int dd = 0; dd < 2; ++dd)
; #pragma unroll
;             for (int g = 0; g < 4; ++g) {
;                 float p[4], q[4];
; #pragma unroll
;                 for (int j = 0; j < 4; ++j) { const float c = zc[dd][4 * g + j], s = zs[dd][4 * g + j]; p[j] = c * t2.x - s * t2.y; q[j] = c * t2.y + s * t2.x; }
;                 u32x2 wp, wq; wp.x = cvt_pk_bf16(p[0], p[1]); wp.y = cvt_pk_bf16(p[2], p[3]); wq.x = cvt_pk_bf16(q[0], q[1]); wq.y = cvt_pk_bf16(q[2], q[3]);
;                 *(u32x2*)(zp + dd * 32 + 8 * g) = wp; *(u32x2*)(zp + 512 + dd * 32 + 8 * g) = wq;
	v_pk_mul_f32 v[50:51], v[50:51], v[116:117]
	v_pk_mul_f32 v[34:35], v[34:35], v[116:117]
	v_pk_mul_f32 v[132:133], v[132:133], v[116:117]
	v_pk_mul_f32 v[128:129], v[128:129], v[116:117]
	v_pk_mul_f32 v[52:53], v[52:53], v[116:117]
	v_pk_mul_f32 v[36:37], v[36:37], v[116:117]
	v_sub_f32_e32 v50, v50, v51
	v_add_f32_e32 v51, v35, v34
	v_sub_f32_e32 v35, v132, v133
	v_pk_mul_f32 v[130:131], v[130:131], v[116:117]
	v_pk_mul_f32 v[134:135], v[134:135], v[116:117]
	v_pk_mul_f32 v[136:137], v[136:137], v[116:117]
	v_pk_mul_f32 v[54:55], v[54:55], v[116:117]
	v_pk_mul_f32 v[38:39], v[38:39], v[116:117]
	v_pk_mul_f32 v[140:141], v[140:141], v[116:117]
	v_pk_mul_f32 v[56:57], v[56:57], v[116:117]
	v_sub_f32_e32 v115, v128, v129
	v_sub_f32_e32 v52, v52, v53
	v_add_f32_e32 v37, v37, v36
	v_cvt_pk_bf16_f32 v34, v115, v50
	v_cvt_pk_bf16_f32 v35, v35, v52
	v_pk_mul_f32 v[138:139], v[138:139], v[116:117]
	v_pk_mul_f32 v[142:143], v[142:143], v[116:117]
	v_pk_mul_f32 v[40:41], v[40:41], v[116:117]
	v_add_f32_e32 v127, v131, v130
	v_add_f32_e32 v128, v135, v134
	v_sub_f32_e32 v53, v136, v137
	v_sub_f32_e32 v54, v54, v55
	v_add_f32_e32 v38, v39, v38
	v_sub_f32_e32 v39, v140, v141
	v_sub_f32_e32 v56, v56, v57
	v_cvt_pk_bf16_f32 v36, v127, v51
	v_cvt_pk_bf16_f32 v37, v128, v37
	ds_write_b64 v176, v[34:35]
	ds_write_b64 v176, v[36:37] offset:128
	v_cvt_pk_bf16_f32 v34, v53, v54
	v_cvt_pk_bf16_f32 v35, v39, v56
	v_add_f32_e32 v129, v139, v138
	v_add_f32_e32 v55, v143, v142
	v_add_f32_e32 v40, v41, v40
	v_cvt_pk_bf16_f32 v36, v129, v38
	v_cvt_pk_bf16_f32 v37, v55, v40
	ds_write_b64 v176, v[34:35] offset:16
	ds_write_b64 v176, v[36:37] offset:144
	v_mov_b32_e32 v34, v42
	v_mov_b32_e32 v35, v58
	v_pk_mul_f32 v[34:35], v[34:35], v[116:117]
	v_mfma_f32_32x32x16_bf16 v[2:17], v[172:175], v[152:155], v[2:17]
	v_sub_f32_e32 v36, v34, v35
	v_mov_b32_e32 v34, v58
	v_mov_b32_e32 v35, v42
	v_mul_f32_e64 v34, v34, v116
	v_mul_f32_e64 v35, v35, v117
	v_mov_b32_e32 v58, v43
	v_add_f32_e32 v37, v35, v34
	v_pk_mul_f32 v[34:35], v[58:59], v[116:117]
	v_mov_b32_e32 v42, v59
	v_sub_f32_e32 v38, v34, v35
	v_pk_mul_f32 v[34:35], v[42:43], v[116:117]
	v_mfma_f32_32x32x16_bf16 v[18:33], v[172:175], v[156:159], v[18:33]
	v_add_f32_e32 v39, v35, v34
	v_mov_b32_e32 v34, v44
	v_mov_b32_e32 v35, v60
	v_mul_f32_e64 v34, v34, v116
	v_mul_f32_e64 v35, v35, v117
	v_sub_f32_e32 v40, v34, v35
	v_mov_b32_e32 v34, v60
	v_mov_b32_e32 v35, v44
	v_pk_mul_f32 v[34:35], v[34:35], v[116:117]
	v_mov_b32_e32 v60, v45
	v_add_f32_e32 v41, v35, v34
	v_pk_mul_f32 v[34:35], v[60:61], v[116:117]
	v_mov_b32_e32 v44, v61
	v_sub_f32_e32 v42, v34, v35
	v_pk_mul_f32 v[34:35], v[44:45], v[116:117]
	s_nop 0
	v_add_f32_e32 v43, v35, v34
	v_cvt_pk_bf16_f32 v34, v36, v38
	v_cvt_pk_bf16_f32 v35, v40, v42
	v_cvt_pk_bf16_f32 v36, v37, v39
	v_cvt_pk_bf16_f32 v37, v41, v43
	ds_write_b64 v176, v[34:35] offset:32
	ds_write_b64 v176, v[36:37] offset:160
	v_mov_b32_e32 v34, v46
	v_mov_b32_e32 v35, v62
	v_pk_mul_f32 v[34:35], v[34:35], v[116:117]
	s_nop 0
	v_sub_f32_e32 v36, v34, v35
	v_mov_b32_e32 v34, v62
	v_mov_b32_e32 v35, v46
	v_pk_mul_f32 v[34:35], v[34:35], v[116:117]
	v_mov_b32_e32 v62, v47
	v_add_f32_e32 v37, v35, v34
	v_pk_mul_f32 v[34:35], v[62:63], v[116:117]
	v_mov_b32_e32 v46, v63
	v_sub_f32_e32 v38, v34, v35
	v_pk_mul_f32 v[34:35], v[46:47], v[116:117]
	s_nop 0
	v_add_f32_e32 v39, v35, v34
	v_mov_b32_e32 v34, v48
	v_mov_b32_e32 v35, v64
	v_pk_mul_f32 v[34:35], v[34:35], v[116:117]
	s_nop 0
	v_sub_f32_e32 v40, v34, v35
	v_mov_b32_e32 v34, v64
	v_mov_b32_e32 v35, v48
	v_pk_mul_f32 v[34:35], v[34:35], v[116:117]
	v_mov_b32_e32 v64, v49
	v_add_f32_e32 v41, v35, v34
	v_pk_mul_f32 v[34:35], v[64:65], v[116:117]
	v_mov_b32_e32 v48, v65
	v_sub_f32_e32 v42, v34, v35
	v_pk_mul_f32 v[34:35], v[48:49], v[116:117]
	s_nop 0
	v_add_f32_e32 v43, v35, v34
	v_cvt_pk_bf16_f32 v34, v36, v38
	v_cvt_pk_bf16_f32 v35, v40, v42
	v_cvt_pk_bf16_f32 v36, v37, v39
	v_cvt_pk_bf16_f32 v37, v41, v43
	ds_write_b64 v176, v[34:35] offset:48
	ds_write_b64 v176, v[36:37] offset:176
	v_mov_b32_e32 v34, v2
	v_mov_b32_e32 v35, v18
	v_pk_mul_f32 v[34:35], v[34:35], v[116:117]
	s_nop 0
	v_sub_f32_e32 v36, v34, v35
	v_mov_b32_e32 v34, v18
	v_mov_b32_e32 v35, v2
	v_mov_b32_e32 v2, v19
	v_pk_mul_f32 v[34:35], v[34:35], v[116:117]
	v_mov_b32_e32 v18, v3
	v_pk_mul_f32 v[2:3], v[2:3], v[116:117]
	v_add_f32_e32 v37, v35, v34
	v_pk_mul_f32 v[34:35], v[18:19], v[116:117]
	v_add_f32_e32 v19, v3, v2
	v_mov_b32_e32 v2, v4
	v_mov_b32_e32 v3, v20
	v_pk_mul_f32 v[2:3], v[2:3], v[116:117]
	v_sub_f32_e32 v18, v34, v35
	v_sub_f32_e32 v34, v2, v3
	v_mov_b32_e32 v2, v20
	v_mov_b32_e32 v3, v4
	v_pk_mul_f32 v[2:3], v[2:3], v[116:117]
	v_mov_b32_e32 v20, v5
	v_add_f32_e32 v35, v3, v2
; __device__ __forceinline__ unsigned cvt_pk_bf16(float lo, float hi) { unsigned r; asm volatile("v_cvt_pk_bf16_f32 %0, %1, %2" : "=v"(r) : "v"(lo), "v"(hi)); return r; }
; __device__ __forceinline__ void phase_fft_a(const Frame& F) {
;     ...
; #pragma unroll
;         for (int dd = 0; dd < 2; ++dd)
; #pragma unroll
;             for (int g = 0; g < 4; ++g) {
;                 float p[4], q[4];
; #pragma unroll
;                 for (int j = 0; j < 4; ++j) { const float c = zc[dd][4 * g + j], s = zs[dd][4 * g + j]; p[j] = c * t2.x - s * t2.y; q[j] = c * t2.y + s * t2.x; }
;                 u32x2 wp, wq; wp.x = cvt_pk_bf16(p[0], p[1]); wp.y = cvt_pk_bf16(p[2], p[3]); wq.x = cvt_pk_bf16(q[0], q[1]); wq.y = cvt_pk_bf16(q[2], q[3]);
;                 *(u32x2*)(zp + dd * 32 + 8 * g) = wp; *(u32x2*)(zp + 512 + dd * 32 + 8 * g) = wq;
	v_pk_mul_f32 v[2:3], v[20:21], v[116:117]
	v_mov_b32_e32 v4, v21
	v_sub_f32_e32 v20, v2, v3
	v_pk_mul_f32 v[2:3], v[4:5], v[116:117]
	s_nop 0
	v_add_f32_e32 v5, v3, v2
	v_cvt_pk_bf16_f32 v2, v36, v18
	v_cvt_pk_bf16_f32 v3, v34, v20
	v_cvt_pk_bf16_f32 v4, v37, v19
	v_cvt_pk_bf16_f32 v5, v35, v5
	ds_write_b64 v176, v[2:3] offset:64
	ds_write_b64 v176, v[4:5] offset:192
	v_mov_b32_e32 v2, v6
	v_mov_b32_e32 v3, v22
	v_pk_mul_f32 v[2:3], v[2:3], v[116:117]
	s_nop 0
	v_sub_f32_e32 v4, v2, v3
	v_mov_b32_e32 v2, v22
	v_mov_b32_e32 v3, v6
	v_pk_mul_f32 v[2:3], v[2:3], v[116:117]
	v_mov_b32_e32 v22, v7
	v_add_f32_e32 v5, v3, v2
	v_pk_mul_f32 v[2:3], v[22:23], v[116:117]
	v_mov_b32_e32 v6, v23
	v_sub_f32_e32 v18, v2, v3
	v_pk_mul_f32 v[2:3], v[6:7], v[116:117]
	s_nop 0
	v_add_f32_e32 v6, v3, v2
	v_mov_b32_e32 v2, v8
	v_mov_b32_e32 v3, v24
	v_pk_mul_f32 v[2:3], v[2:3], v[116:117]
	s_nop 0
	v_sub_f32_e32 v7, v2, v3
	v_mov_b32_e32 v2, v24
	v_mov_b32_e32 v3, v8
	v_pk_mul_f32 v[2:3], v[2:3], v[116:117]
	v_mov_b32_e32 v24, v9
	v_add_f32_e32 v19, v3, v2
	v_pk_mul_f32 v[2:3], v[24:25], v[116:117]
	v_mov_b32_e32 v8, v25
	v_sub_f32_e32 v20, v2, v3
	v_pk_mul_f32 v[2:3], v[8:9], v[116:117]
	s_nop 0
	v_add_f32_e32 v8, v3, v2
	v_cvt_pk_bf16_f32 v2, v4, v18
	v_cvt_pk_bf16_f32 v3, v7, v20
	v_cvt_pk_bf16_f32 v4, v5, v6
	v_cvt_pk_bf16_f32 v5, v19, v8
	ds_write_b64 v176, v[2:3] offset:80
	ds_write_b64 v176, v[4:5] offset:208
	v_mov_b32_e32 v2, v10
	v_mov_b32_e32 v3, v26
	v_pk_mul_f32 v[2:3], v[2:3], v[116:117]
	s_nop 0
	v_sub_f32_e32 v4, v2, v3
	v_mov_b32_e32 v2, v26
	v_mov_b32_e32 v3, v10
	v_pk_mul_f32 v[2:3], v[2:3], v[116:117]
	v_mov_b32_e32 v26, v11
	v_add_f32_e32 v5, v3, v2
	v_pk_mul_f32 v[2:3], v[26:27], v[116:117]
	v_mov_b32_e32 v10, v27
	v_sub_f32_e32 v6, v2, v3
	v_pk_mul_f32 v[2:3], v[10:11], v[116:117]
	s_nop 0
	v_add_f32_e32 v7, v3, v2
	v_mov_b32_e32 v2, v12
	v_mov_b32_e32 v3, v28
	v_pk_mul_f32 v[2:3], v[2:3], v[116:117]
	s_nop 0
	v_sub_f32_e32 v8, v2, v3
	v_mov_b32_e32 v2, v28
	v_mov_b32_e32 v3, v12
	v_pk_mul_f32 v[2:3], v[2:3], v[116:117]
	v_mov_b32_e32 v28, v13
	v_add_f32_e32 v9, v3, v2
	v_pk_mul_f32 v[2:3], v[28:29], v[116:117]
	v_mov_b32_e32 v12, v29
	v_sub_f32_e32 v10, v2, v3
	v_pk_mul_f32 v[2:3], v[12:13], v[116:117]
	s_nop 0
	v_add_f32_e32 v11, v3, v2
	v_cvt_pk_bf16_f32 v2, v4, v6
	v_cvt_pk_bf16_f32 v3, v8, v10
	v_cvt_pk_bf16_f32 v4, v5, v7
	v_cvt_pk_bf16_f32 v5, v9, v11
	ds_write_b64 v176, v[2:3] offset:96
	ds_write_b64 v176, v[4:5] offset:224
	v_mov_b32_e32 v2, v14
	v_mov_b32_e32 v3, v30
	v_pk_mul_f32 v[2:3], v[2:3], v[116:117]
	s_nop 0
	v_sub_f32_e32 v4, v2, v3
	v_mov_b32_e32 v2, v30
	v_mov_b32_e32 v3, v14
	v_pk_mul_f32 v[2:3], v[2:3], v[116:117]
	v_mov_b32_e32 v30, v15
	v_add_f32_e32 v5, v3, v2
	v_pk_mul_f32 v[2:3], v[30:31], v[116:117]
	v_mov_b32_e32 v14, v31
	v_sub_f32_e32 v6, v2, v3
	v_pk_mul_f32 v[2:3], v[14:15], v[116:117]
	s_nop 0
	v_add_f32_e32 v7, v3, v2
	v_mov_b32_e32 v2, v16
	v_mov_b32_e32 v3, v32
	v_pk_mul_f32 v[2:3], v[2:3], v[116:117]
	s_nop 0
	v_sub_f32_e32 v8, v2, v3
	v_mov_b32_e32 v2, v32
	v_mov_b32_e32 v3, v16
	v_pk_mul_f32 v[2:3], v[2:3], v[116:117]
	v_mov_b32_e32 v32, v17
	v_add_f32_e32 v9, v3, v2
	v_pk_mul_f32 v[2:3], v[32:33], v[116:117]
	v_mov_b32_e32 v16, v33
	v_sub_f32_e32 v10, v2, v3
	v_pk_mul_f32 v[2:3], v[16:17], v[116:117]
	s_nop 0
	v_add_f32_e32 v11, v3, v2
	v_cvt_pk_bf16_f32 v2, v4, v6
	v_cvt_pk_bf16_f32 v3, v8, v10
	v_cvt_pk_bf16_f32 v4, v5, v7
	v_cvt_pk_bf16_f32 v5, v9, v11
	ds_write_b64 v176, v[2:3] offset:112
	ds_write_b64 v176, v[4:5] offset:240
	s_waitcnt lgkmcnt(0)
	ds_read_b128 v[184:187], v177
	ds_read_b128 v[188:191], v177 offset:2176
	ds_read_b128 v[192:195], v177 offset:4352
	ds_read_b128 v[198:201], v177 offset:6528
	ds_read_b128 v[202:205], v177 offset:128
	ds_read_b128 v[206:209], v177 offset:2304
	ds_read_b128 v[210:213], v177 offset:4480
	ds_read_b128 v[214:217], v177 offset:6656
	s_mov_b64 s[100:101], 0x100000
	v_lshl_add_u64 v[178:179], v[118:119], 0, s[100:101]
	v_lshl_add_u64 v[180:181], v[178:179], 0, s[100:101]
	v_lshl_add_u64 v[182:183], v[180:181], 0, s[100:101]
	s_waitcnt lgkmcnt(7)
	global_store_dwordx4 v[118:119], v[184:187], off
	s_waitcnt lgkmcnt(6)
	global_store_dwordx4 v[178:179], v[188:191], off
	s_waitcnt lgkmcnt(5)
	global_store_dwordx4 v[180:181], v[192:195], off
	s_waitcnt lgkmcnt(4)
	global_store_dwordx4 v[182:183], v[198:201], off
	s_waitcnt lgkmcnt(3)
	global_store_dwordx4 v[118:119], v[202:205], off offset:1024
	s_waitcnt lgkmcnt(2)
	global_store_dwordx4 v[178:179], v[206:209], off offset:1024
	s_waitcnt lgkmcnt(1)
	global_store_dwordx4 v[180:181], v[210:213], off offset:1024
	s_waitcnt lgkmcnt(0)
	global_store_dwordx4 v[182:183], v[214:217], off offset:1024
	s_cbranch_vccz .LBB0_331
